# attention steady loop: the K(t+2) LDS-DMA issue moved from the step head into the QK MFMA run (after MFMA 2 and 4); GEMM unit-boundary peel kept
# baseline (speedup 1.0000x reference)
.LBB0_432:
	v_lshl_add_u64 v[178:179], v[190:191], 0, s[92:93]
	v_lshl_add_u64 v[240:241], v[178:179], 0, s[96:97]
	s_add_i32 s26, s9, s69
	v_lshl_add_u64 v[242:243], v[178:179], 0, s[4:5]
	s_add_i32 s27, s26, 0x2000
	v_add_u32_e32 v80, s8, v224
	v_add_u32_e32 v180, s9, v222
	ds_read_b128 v[116:119], v80 offset:4096
	ds_read_b128 v[120:123], v80 offset:4608
	ds_read_b64_tr_b16 v[174:175], v180 offset:49152
	ds_read_b64_tr_b16 v[176:177], v180 offset:49664
	s_waitcnt lgkmcnt(7)
	v_mfma_f32_32x32x16_bf16 v[96:111], v[170:173], v[154:157], v[64:79]
	ds_read_b128 v[182:185], v80 offset:6144
	ds_read_b128 v[200:203], v80 offset:6656
	s_waitcnt lgkmcnt(8)
	v_mfma_f32_32x32x16_bf16 v[80:95], v[162:165], v[154:157], v[64:79]
	ds_read_b64_tr_b16 v[170:171], v180 offset:53248
	ds_read_b64_tr_b16 v[172:173], v180 offset:53760
	s_mov_b32 m0, s26
	s_nop 0
	global_load_lds_dwordx4 v[240:241], off
	s_waitcnt lgkmcnt(9)
	v_mfma_f32_32x32x16_bf16 v[96:111], v[166:169], v[150:153], v[96:111]
	ds_read_b64_tr_b16 v[166:167], v180 offset:57344
	ds_read_b64_tr_b16 v[168:169], v180 offset:57856
	s_waitcnt lgkmcnt(10)
	v_mfma_f32_32x32x16_bf16 v[80:95], v[158:161], v[150:153], v[80:95]
	ds_read_b64_tr_b16 v[162:163], v180 offset:61440
	ds_read_b64_tr_b16 v[164:165], v180 offset:61952
	s_mov_b32 m0, s27
	s_nop 0
	global_load_lds_dwordx4 v[242:243], off
	s_waitcnt lgkmcnt(11)
	v_mfma_f32_32x32x16_bf16 v[96:111], v[116:119], v[146:149], v[96:111]
	ds_read_b64_tr_b16 v[158:159], v180 offset:50176
	ds_read_b64_tr_b16 v[160:161], v180 offset:50688
	s_waitcnt lgkmcnt(12)
	v_mfma_f32_32x32x16_bf16 v[80:95], v[120:123], v[146:149], v[80:95]
	ds_read_b64_tr_b16 v[124:125], v180 offset:54272
	ds_read_b64_tr_b16 v[126:127], v180 offset:54784
	s_waitcnt lgkmcnt(11)
	v_mfma_f32_32x32x16_bf16 v[96:111], v[182:185], v[142:145], v[96:111]
	ds_read_b64_tr_b16 v[120:121], v180 offset:58368
	ds_read_b64_tr_b16 v[122:123], v180 offset:58880
	s_waitcnt lgkmcnt(12)
	v_mfma_f32_32x32x16_bf16 v[80:95], v[200:203], v[142:145], v[80:95]
	ds_read_b64_tr_b16 v[116:117], v180 offset:62464
	ds_read_b64_tr_b16 v[118:119], v180 offset:62976
	v_lshl_add_u64 v[194:195], v[192:193], 0, s[92:93]
	v_lshl_add_u64 v[182:183], v[194:195], 0, s[28:29]
	s_add_i32 s9, s76, s70
	v_lshl_add_u64 v[184:185], v[194:195], 0, s[86:87]
	s_add_i32 s26, s9, 0x2000
	s_mov_b32 m0, s9
	s_nop 0
	global_load_lds_dwordx4 v[182:183], off
	s_mov_b32 m0, s26
	s_nop 0
	global_load_lds_dwordx4 v[184:185], off
	s_nop 0
	v_max_f32_e32 v181, v97, v97
	v_max_f32_e32 v182, v96, v96
	v_max_f32_e32 v181, v182, v181
	s_nop 0
	v_max3_f32 v182, v98, v99, v81
	v_max3_f32 v181, v181, v80, v82
	v_max3_f32 v181, v181, v83, v100
	v_max3_f32 v182, v182, v102, v103
	v_max3_f32 v181, v181, v101, v84
	v_max3_f32 v182, v182, v86, v87
	v_max3_f32 v181, v181, v85, v104
	v_max3_f32 v182, v182, v106, v107
	v_max3_f32 v181, v181, v105, v88
	v_max3_f32 v182, v182, v90, v91
	v_max3_f32 v181, v181, v89, v108
	v_max3_f32 v182, v182, v110, v111
	v_max3_f32 v181, v181, v109, v92
	v_max3_f32 v182, v182, v94, v95
	v_max3_f32 v181, v181, v93, v182
	v_mov_b32_e32 v182, v181
	s_nop 1
	v_permlane32_swap_b32_e32 v181, v182
	v_max_f32_e32 v182, v182, v182
	v_max_f32_e32 v181, v181, v181
	v_max_f32_e32 v181, v181, v182
	v_cmp_lt_f32_e32 vcc, s13, v181
	s_cmp_lg_u64 vcc, 0
	s_cselect_b64 s[26:27], -1, 0
	s_cbranch_vccnz .LBB0_440

.LBB0_435:
	v_add_f32_e32 v80, v92, v93
	v_add_f32_e32 v80, v101, v80
	v_add_f32_e32 v81, v94, v95
	s_add_i32 s9, s76, 0x4000
	v_add_f32_e32 v80, v81, v80
	s_cmpk_lg_u32 s76, 0x8000
	v_add_f32_e32 v189, v226, v80
	s_cselect_b32 s39, s9, 0
	s_mov_b64 s[26:27], 0x7380800
	v_lshl_add_u64 v[244:245], v[178:179], 0, s[26:27]
	s_mov_b64 s[26:27], 0x7380880
	s_add_i32 s9, s8, s69
	v_lshl_add_u64 v[246:247], v[178:179], 0, s[26:27]
	s_add_i32 s26, s9, 0x2000
	v_add_u32_e32 v200, s8, v222
	ds_read_b128 v[80:83], v100 offset:4096
	ds_read_b128 v[84:87], v100 offset:4608
	ds_read_b64_tr_b16 v[182:183], v200 offset:49152
	ds_read_b64_tr_b16 v[184:185], v200 offset:49664
	s_waitcnt lgkmcnt(7)
	v_mfma_f32_32x32x16_bf16 v[112:127], v[96:99], v[154:157], v[64:79]
	ds_read_b128 v[202:205], v100 offset:6144
	ds_read_b128 v[228:231], v100 offset:6656
	s_waitcnt lgkmcnt(8)
	v_mfma_f32_32x32x16_bf16 v[96:111], v[158:161], v[154:157], v[64:79]
	ds_read_b64_tr_b16 v[178:179], v200 offset:53248
	ds_read_b64_tr_b16 v[180:181], v200 offset:53760
	s_mov_b32 m0, s9
	s_nop 0
	global_load_lds_dwordx4 v[244:245], off
	s_waitcnt lgkmcnt(9)
	v_mfma_f32_32x32x16_bf16 v[112:127], v[166:169], v[150:153], v[112:127]
	ds_read_b64_tr_b16 v[174:175], v200 offset:57344
	ds_read_b64_tr_b16 v[176:177], v200 offset:57856
	s_waitcnt lgkmcnt(10)
	v_mfma_f32_32x32x16_bf16 v[96:111], v[162:165], v[150:153], v[96:111]
	ds_read_b64_tr_b16 v[170:171], v200 offset:61440
	ds_read_b64_tr_b16 v[172:173], v200 offset:61952
	s_mov_b32 m0, s26
	s_nop 0
	global_load_lds_dwordx4 v[246:247], off
	s_waitcnt lgkmcnt(11)
	v_mfma_f32_32x32x16_bf16 v[112:127], v[80:83], v[146:149], v[112:127]
	ds_read_b64_tr_b16 v[166:167], v200 offset:50176
	ds_read_b64_tr_b16 v[168:169], v200 offset:50688
	s_waitcnt lgkmcnt(12)
	v_mfma_f32_32x32x16_bf16 v[96:111], v[84:87], v[146:149], v[96:111]
	ds_read_b64_tr_b16 v[162:163], v200 offset:54272
	ds_read_b64_tr_b16 v[164:165], v200 offset:54784
	s_waitcnt lgkmcnt(11)
	v_mfma_f32_32x32x16_bf16 v[112:127], v[202:205], v[142:145], v[112:127]
	ds_read_b64_tr_b16 v[158:159], v200 offset:58368
	ds_read_b64_tr_b16 v[160:161], v200 offset:58880
	s_waitcnt lgkmcnt(12)
	v_mfma_f32_32x32x16_bf16 v[96:111], v[228:231], v[142:145], v[96:111]
	ds_read_b64_tr_b16 v[84:85], v200 offset:62464
	ds_read_b64_tr_b16 v[86:87], v200 offset:62976
	s_mov_b64 s[8:9], 0x7321000
	v_lshl_add_u64 v[80:81], v[194:195], 0, s[8:9]
	s_mov_b64 s[8:9], 0x7321080
	v_lshl_add_u64 v[82:83], v[194:195], 0, s[8:9]
	s_add_i32 s8, s39, s70
	s_add_i32 s9, s8, 0x2000
	s_mov_b32 m0, s8
	s_nop 0
	global_load_lds_dwordx4 v[80:81], off
	s_mov_b32 m0, s9
	s_nop 0
	global_load_lds_dwordx4 v[82:83], off
	v_max_f32_e32 v80, v113, v113
	v_max_f32_e32 v81, v112, v112
	v_max_f32_e32 v80, v81, v80
	s_nop 0
	v_max3_f32 v81, v114, v115, v97
	v_max3_f32 v80, v80, v96, v98
	v_max3_f32 v80, v80, v99, v116
	v_max3_f32 v81, v81, v118, v119
	v_max3_f32 v80, v80, v117, v100
	v_max3_f32 v81, v81, v102, v103
	v_max3_f32 v80, v80, v101, v120
	v_max3_f32 v81, v81, v122, v123
	v_max3_f32 v80, v80, v121, v104
	v_max3_f32 v81, v81, v106, v107
	v_max3_f32 v80, v80, v105, v124
	v_max3_f32 v81, v81, v126, v127
	v_max3_f32 v80, v80, v125, v108
	v_max3_f32 v81, v81, v110, v111
	v_max3_f32 v80, v80, v109, v81
	v_mov_b32_e32 v81, v80
	s_nop 1
	v_permlane32_swap_b32_e32 v80, v81
	v_max_f32_e32 v81, v81, v81
	v_max_f32_e32 v80, v80, v80
	v_max_f32_e32 v80, v80, v81
	v_cmp_lt_f32_e32 vcc, s13, v80
	s_cmp_lg_u64 vcc, 0
	s_cselect_b64 s[26:27], -1, 0
	s_cbranch_vccnz .LBB0_443
